# best + nt on P6 out-projection output stores only
# baseline (speedup 1.0000x reference)
; #define LAS __attribute__((address_space(3)))
; #define EPS_LOAD(g_) do { const size_t off_ = (size_t)(row0 + ((g_) >> 2) * HALF + ((g_) & 3) * 16) * ldc + col0; \
;             _Pragma("unroll") for (int bj = 0; bj < 2; ++bj) _Pragma("unroll") for (int n = 0; n < 2; ++n) rb[(g_) & 3][2 * bj + n] = *(const f32x4*)(base + off_ + bj * HALF + n * 16); } while (0)
;     DI void operator()(const f32x4 (&acc)[2][2][4][2], const Unit& u, int wr, int wc, int fr, int fq, const LAS unsigned char* st) const {
;         const int row0 = u.pm * BM + wr * 64 + fr, col0 = u.pn * BM + wc * 32 + 4 * fq;
;         f32x4 rb[4][4];
;     ...
;         EPS_LOAD(0); EPS_LOAD(1); EPS_LOAD(2);
; #pragma unroll
;         for (int ai = 0; ai < 2; ++ai)
; #pragma unroll
;             for (int m = 0; m < 4; ++m) { const int g = 4 * ai + m; const size_t off = (size_t)(row0 + ai * HALF + m * 16) * ldc + col0;
;                 if (g + 3 < 8) EPS_LOAD(g + 3);
; #pragma unroll
;                 for (int bj = 0; bj < 2; ++bj)
; #pragma unroll
;                     for (int n = 0; n < 2; ++n) *(f32x4*)(C + off + bj * HALF + n * 16) = rb[g & 3][2 * bj + n] + acc[ai][bj][m][n]; }
.LBB0_796:
	v_mov_b32_e32 v130, v224
	s_lshl_b32 s0, s28, 8
	s_add_i32 s0, s0, s45
	v_and_or_b32 v140, v130, 15, s0
	s_lshl_b32 s0, s54, 8
	v_ashrrev_i32_e32 v130, 2, v130
	s_or_b32 s0, s0, s46
	v_and_b32_e32 v130, -4, v130
	v_add_u32_e32 v136, s0, v130
	v_ashrrev_i32_e32 v141, 31, v140
	v_readlane_b32 s0, v254, 3
	v_or_b32_e32 v168, 16, v140
	v_or_b32_e32 v184, 32, v140
	v_ashrrev_i32_e32 v137, 31, v136
	v_lshlrev_b64 v[138:139], 13, v[140:141]
	v_readlane_b32 s1, v254, 4
	v_ashrrev_i32_e32 v169, 31, v168
	v_ashrrev_i32_e32 v185, 31, v184
	v_lshl_add_u64 v[152:153], s[0:1], 0, v[138:139]
	v_lshlrev_b64 v[136:137], 2, v[136:137]
	v_lshlrev_b64 v[216:217], 13, v[168:169]
	v_lshlrev_b64 v[218:219], 13, v[184:185]
	v_lshl_add_u64 v[164:165], v[152:153], 0, v[136:137]
	v_lshl_add_u64 v[168:169], s[0:1], 0, v[216:217]
	v_lshl_add_u64 v[184:185], s[0:1], 0, v[218:219]
	global_load_dwordx4 v[152:155], v[164:165], off
	global_load_dwordx4 v[156:159], v[164:165], off offset:64
	global_load_dwordx4 v[160:163], v[164:165], off offset:512
	s_nop 0
	global_load_dwordx4 v[164:167], v[164:165], off offset:576
	v_lshl_add_u64 v[180:181], v[168:169], 0, v[136:137]
	v_lshl_add_u64 v[196:197], v[184:185], 0, v[136:137]
	global_load_dwordx4 v[168:171], v[180:181], off
	global_load_dwordx4 v[172:175], v[180:181], off offset:64
	global_load_dwordx4 v[176:179], v[180:181], off offset:512
	s_nop 0
	global_load_dwordx4 v[180:183], v[180:181], off offset:576
	s_nop 0
	global_load_dwordx4 v[184:187], v[196:197], off
	global_load_dwordx4 v[188:191], v[196:197], off offset:64
	global_load_dwordx4 v[192:195], v[196:197], off offset:512
	s_nop 0
	global_load_dwordx4 v[196:199], v[196:197], off offset:576
	v_or_b32_e32 v200, 48, v140
	v_ashrrev_i32_e32 v201, 31, v200
	v_lshlrev_b64 v[220:221], 13, v[200:201]
	v_lshl_add_u64 v[200:201], s[0:1], 0, v[220:221]
	v_lshl_add_u64 v[212:213], v[200:201], 0, v[136:137]
	global_load_dwordx4 v[200:203], v[212:213], off
	global_load_dwordx4 v[204:207], v[212:213], off offset:64
	global_load_dwordx4 v[208:211], v[212:213], off offset:512
	s_nop 0
	global_load_dwordx4 v[212:215], v[212:213], off offset:576
	v_lshl_add_u64 v[222:223], s[92:93], 0, v[138:139]
	v_lshl_add_u64 v[226:227], v[138:139], 0, s[74:75]
	v_lshl_add_u64 v[228:229], v[138:139], 0, s[76:77]
	v_lshl_add_u64 v[230:231], s[0:1], 0, v[226:227]
	v_lshl_add_u64 v[216:217], s[92:93], 0, v[216:217]
	v_lshl_add_u64 v[138:139], v[222:223], 0, v[136:137]
	v_lshl_add_u64 v[232:233], s[0:1], 0, v[228:229]
	v_lshl_add_u64 v[218:219], s[92:93], 0, v[218:219]
	v_lshl_add_u64 v[222:223], v[230:231], 0, v[136:137]
	v_lshl_add_u64 v[216:217], v[216:217], 0, v[136:137]
	v_lshl_add_u64 v[230:231], v[232:233], 0, v[136:137]
	v_readlane_b32 s2, v254, 5
	v_readlane_b32 s3, v254, 6
	v_readlane_b32 s4, v254, 7
	v_readlane_b32 s5, v254, 8
	v_readlane_b32 s6, v254, 9
	v_readlane_b32 s7, v254, 10
	v_readlane_b32 s8, v254, 11
	v_readlane_b32 s9, v254, 12
	v_readlane_b32 s10, v254, 13
	v_readlane_b32 s11, v254, 14
	v_readlane_b32 s12, v254, 15
	v_readlane_b32 s13, v254, 16
	v_readlane_b32 s14, v254, 17
	v_readlane_b32 s15, v254, 18
	s_waitcnt vmcnt(0)
	v_pk_add_f32 v[128:129], v[128:129], v[154:155]
	v_pk_add_f32 v[126:127], v[126:127], v[152:153]
	v_pk_add_f32 v[124:125], v[124:125], v[158:159]
	v_pk_add_f32 v[122:123], v[122:123], v[156:157]
	v_pk_add_f32 v[108:109], v[108:109], v[162:163]
	v_pk_add_f32 v[106:107], v[106:107], v[160:161]
	v_pk_add_f32 v[104:105], v[104:105], v[166:167]
	v_pk_add_f32 v[102:103], v[102:103], v[164:165]
	v_pk_add_f32 v[120:121], v[120:121], v[170:171]
	v_pk_add_f32 v[118:119], v[118:119], v[168:169]
	global_store_dwordx4 v[138:139], v[126:129], off nt
	global_store_dwordx4 v[138:139], v[122:125], off offset:64 nt
	global_store_dwordx4 v[138:139], v[106:109], off offset:512 nt
	global_store_dwordx4 v[138:139], v[102:105], off offset:576 nt
	v_pk_add_f32 v[116:117], v[116:117], v[174:175]
	v_pk_add_f32 v[114:115], v[114:115], v[172:173]
	v_pk_add_f32 v[100:101], v[100:101], v[178:179]
	v_pk_add_f32 v[98:99], v[98:99], v[176:177]
	v_pk_add_f32 v[96:97], v[96:97], v[182:183]
	v_pk_add_f32 v[94:95], v[94:95], v[180:181]
	global_load_dwordx4 v[102:105], v[222:223], off
	global_load_dwordx4 v[106:109], v[222:223], off offset:64
	global_load_dwordx4 v[122:125], v[222:223], off offset:512
	global_load_dwordx4 v[126:129], v[222:223], off offset:576
	s_nop 0
	global_store_dwordx4 v[216:217], v[118:121], off nt
	global_store_dwordx4 v[216:217], v[114:117], off offset:64 nt
	global_store_dwordx4 v[216:217], v[98:101], off offset:512 nt
	global_store_dwordx4 v[216:217], v[94:97], off offset:576 nt
	v_lshl_add_u64 v[152:153], v[218:219], 0, v[136:137]
	v_pk_add_f32 v[80:81], v[80:81], v[198:199]
	v_pk_add_f32 v[78:79], v[78:79], v[196:197]
	global_load_dwordx4 v[94:97], v[230:231], off
	global_load_dwordx4 v[98:101], v[230:231], off offset:64
	global_load_dwordx4 v[114:117], v[230:231], off offset:512
	global_load_dwordx4 v[118:121], v[230:231], off offset:576
	v_pk_add_f32 v[112:113], v[112:113], v[186:187]
	global_store_dwordx4 v[152:153], v[78:81], off offset:576 nt
; #define LAS __attribute__((address_space(3)))
; #define EPS_LOAD(g_) do { const size_t off_ = (size_t)(row0 + ((g_) >> 2) * HALF + ((g_) & 3) * 16) * ldc + col0; \
;             _Pragma("unroll") for (int bj = 0; bj < 2; ++bj) _Pragma("unroll") for (int n = 0; n < 2; ++n) rb[(g_) & 3][2 * bj + n] = *(const f32x4*)(base + off_ + bj * HALF + n * 16); } while (0)
;     DI void operator()(const f32x4 (&acc)[2][2][4][2], const Unit& u, int wr, int wc, int fr, int fq, const LAS unsigned char* st) const {
;         const int row0 = u.pm * BM + wr * 64 + fr, col0 = u.pn * BM + wc * 32 + 4 * fq;
;         f32x4 rb[4][4];
;     ...
;         EPS_LOAD(0); EPS_LOAD(1); EPS_LOAD(2);
; #pragma unroll
;         for (int ai = 0; ai < 2; ++ai)
; #pragma unroll
;             for (int m = 0; m < 4; ++m) { const int g = 4 * ai + m; const size_t off = (size_t)(row0 + ai * HALF + m * 16) * ldc + col0;
;                 if (g + 3 < 8) EPS_LOAD(g + 3);
; #pragma unroll
;                 for (int bj = 0; bj < 2; ++bj)
; #pragma unroll
;                     for (int n = 0; n < 2; ++n) *(f32x4*)(C + off + bj * HALF + n * 16) = rb[g & 3][2 * bj + n] + acc[ai][bj][m][n]; }
	v_pk_add_f32 v[110:111], v[110:111], v[184:185]
	v_pk_add_f32 v[92:93], v[92:93], v[190:191]
	v_add_u32_e32 v78, 0xa0, v140
	v_ashrrev_i32_e32 v79, 31, v78
	v_pk_add_f32 v[90:91], v[90:91], v[188:189]
	v_pk_add_f32 v[88:89], v[88:89], v[194:195]
	v_pk_add_f32 v[86:87], v[86:87], v[192:193]
	v_lshlrev_b64 v[78:79], 13, v[78:79]
	global_store_dwordx4 v[152:153], v[110:113], off nt
	global_store_dwordx4 v[152:153], v[90:93], off offset:64 nt
	global_store_dwordx4 v[152:153], v[86:89], off offset:512 nt
	v_lshl_add_u64 v[78:79], s[0:1], 0, v[78:79]
	v_lshl_add_u64 v[152:153], s[92:93], 0, v[220:221]
	v_lshl_add_u64 v[110:111], v[78:79], 0, v[136:137]
	v_lshl_add_u64 v[152:153], v[152:153], 0, v[136:137]
	v_pk_add_f32 v[68:69], v[68:69], v[214:215]
	v_pk_add_f32 v[66:67], v[66:67], v[212:213]
	global_load_dwordx4 v[78:81], v[110:111], off
	global_load_dwordx4 v[86:89], v[110:111], off offset:64
	global_load_dwordx4 v[90:93], v[110:111], off offset:512
	s_nop 0
	global_load_dwordx4 v[110:113], v[110:111], off offset:576
	v_pk_add_f32 v[84:85], v[84:85], v[202:203]
	global_store_dwordx4 v[152:153], v[66:69], off offset:576 nt
	v_pk_add_f32 v[82:83], v[82:83], v[200:201]
	v_pk_add_f32 v[76:77], v[76:77], v[206:207]
	v_add_u32_e32 v66, 0xb0, v140
	v_ashrrev_i32_e32 v67, 31, v66
	v_lshlrev_b64 v[66:67], 13, v[66:67]
	v_pk_add_f32 v[74:75], v[74:75], v[204:205]
	v_pk_add_f32 v[72:73], v[72:73], v[210:211]
	v_pk_add_f32 v[70:71], v[70:71], v[208:209]
	v_lshl_add_u64 v[66:67], s[0:1], 0, v[66:67]
	global_store_dwordx4 v[152:153], v[82:85], off nt
	global_store_dwordx4 v[152:153], v[74:77], off offset:64 nt
	global_store_dwordx4 v[152:153], v[70:73], off offset:512 nt
	v_lshl_add_u64 v[82:83], v[66:67], 0, v[136:137]
	global_load_dwordx4 v[66:69], v[82:83], off
	global_load_dwordx4 v[70:73], v[82:83], off offset:64
	global_load_dwordx4 v[74:77], v[82:83], off offset:512
	s_nop 0
	global_load_dwordx4 v[82:85], v[82:83], off offset:576
	v_lshl_add_u64 v[140:141], s[92:93], 0, v[226:227]
	v_lshl_add_u64 v[152:153], s[92:93], 0, v[228:229]
	v_lshl_add_u64 v[140:141], v[140:141], 0, v[136:137]
	v_lshl_add_u64 v[136:137], v[152:153], 0, v[136:137]
	v_add_co_u32_e32 v154, vcc, s52, v138
	v_lshl_add_u64 v[152:153], v[138:139], 0, s[16:17]
	s_nop 0
	v_addc_co_u32_e32 v155, vcc, 0, v139, vcc
	s_mov_b64 s[0:1], -1
	s_waitcnt vmcnt(27)
	v_pk_add_f32 v[64:65], v[64:65], v[104:105]
	v_pk_add_f32 v[62:63], v[62:63], v[102:103]
	s_waitcnt vmcnt(26)
	v_pk_add_f32 v[60:61], v[60:61], v[108:109]
	s_waitcnt vmcnt(24)
	v_pk_add_f32 v[40:41], v[40:41], v[128:129]
	v_pk_add_f32 v[38:39], v[38:39], v[126:127]
	v_pk_add_f32 v[58:59], v[58:59], v[106:107]
	v_pk_add_f32 v[48:49], v[48:49], v[124:125]
	v_pk_add_f32 v[46:47], v[46:47], v[122:123]
	global_store_dwordx4 v[140:141], v[62:65], off nt
	global_store_dwordx4 v[140:141], v[58:61], off offset:64 nt
	global_store_dwordx4 v[140:141], v[46:49], off offset:512 nt
	global_store_dwordx4 v[140:141], v[38:41], off offset:576 nt
	s_waitcnt vmcnt(20)
	v_pk_add_f32 v[28:29], v[28:29], v[120:121]
	v_pk_add_f32 v[26:27], v[26:27], v[118:119]
	v_pk_add_f32 v[40:41], v[56:57], v[96:97]
	v_pk_add_f32 v[38:39], v[54:55], v[94:95]
	v_pk_add_f32 v[48:49], v[52:53], v[100:101]
	v_pk_add_f32 v[46:47], v[50:51], v[98:99]
	v_pk_add_f32 v[32:33], v[32:33], v[116:117]
	v_pk_add_f32 v[30:31], v[30:31], v[114:115]
	global_store_dwordx4 v[136:137], v[38:41], off nt
	global_store_dwordx4 v[136:137], v[46:49], off offset:64 nt
	global_store_dwordx4 v[136:137], v[30:33], off offset:512 nt
	global_store_dwordx4 v[136:137], v[26:29], off offset:576 nt
	s_waitcnt vmcnt(17)
	v_pk_add_f32 v[20:21], v[20:21], v[92:93]
	v_pk_add_f32 v[28:29], v[44:45], v[80:81]
	v_pk_add_f32 v[26:27], v[42:43], v[78:79]
	v_pk_add_f32 v[18:19], v[18:19], v[90:91]
	v_pk_add_f32 v[32:33], v[36:37], v[88:89]
	v_pk_add_f32 v[30:31], v[34:35], v[86:87]
	global_store_dwordx4 v[154:155], v[26:29], off nt
	global_store_dwordx4 v[152:153], v[30:33], off offset:64 nt
	global_store_dwordx4 v[152:153], v[18:21], off offset:512 nt
	s_waitcnt vmcnt(19)
	v_pk_add_f32 v[16:17], v[16:17], v[112:113]
	v_pk_add_f32 v[14:15], v[14:15], v[110:111]
	v_add_co_u32_e32 v20, vcc, s53, v138
	global_store_dwordx4 v[152:153], v[14:17], off offset:576 nt
	s_nop 0
	v_addc_co_u32_e32 v21, vcc, 0, v139, vcc
	s_waitcnt vmcnt(15)
	v_pk_add_f32 v[16:17], v[24:25], v[68:69]
	v_pk_add_f32 v[14:15], v[22:23], v[66:67]
	v_lshl_add_u64 v[18:19], v[138:139], 0, s[18:19]
	s_waitcnt vmcnt(14)
	v_pk_add_f32 v[12:13], v[12:13], v[72:73]
	v_pk_add_f32 v[10:11], v[10:11], v[70:71]
	s_waitcnt vmcnt(13)
	v_pk_add_f32 v[8:9], v[8:9], v[76:77]
	v_pk_add_f32 v[6:7], v[6:7], v[74:75]
	s_waitcnt vmcnt(12)
	v_pk_add_f32 v[4:5], v[4:5], v[84:85]
	v_pk_add_f32 v[2:3], v[2:3], v[82:83]
	s_andn2_b64 vcc, exec, s[60:61]
	global_store_dwordx4 v[20:21], v[14:17], off nt
	global_store_dwordx4 v[18:19], v[10:13], off offset:64 nt
	global_store_dwordx4 v[18:19], v[6:9], off offset:512 nt
	global_store_dwordx4 v[18:19], v[2:5], off offset:576 nt
	s_cbranch_vccnz .LBB0_785
	s_andn2_b64 vcc, exec, s[64:65]
	s_cbranch_vccnz .LBB0_784
	s_barrier
	s_branch .LBB0_784
